# seam: non-leader L1 invalidate issued before polling the release word (12 in-loop seams)
# baseline (speedup 1.0000x reference)
.LBB0_285:
	v_readlane_b32 s4, v253, 55
	v_readlane_b32 s5, v253, 56
	v_cvt_f32_u32_e32 v3, v5
	v_sub_u32_e32 v7, 0, v5
	v_rcp_iflag_f32_e32 v3, v3
	s_nop 1
	global_atomic_add v6, v4, v201, s[4:5] sc0
	v_mul_f32_e32 v3, 0x4f7ffffe, v3
	v_cvt_u32_f32_e32 v3, v3
	v_mul_lo_u32 v7, v7, v3
	v_mul_hi_u32 v7, v3, v7
	v_add_u32_e32 v3, v3, v7
	s_waitcnt vmcnt(0)
	v_mul_hi_u32 v3, v6, v3
	v_mul_lo_u32 v7, v3, v5
	v_sub_u32_e32 v7, v6, v7
	v_add_u32_e32 v8, 1, v3
	v_cmp_ge_u32_e32 vcc, v7, v5
	v_add_u32_e32 v6, 1, v6
	s_nop 0
	v_cndmask_b32_e32 v3, v3, v8, vcc
	v_sub_u32_e32 v8, v7, v5
	v_cndmask_b32_e32 v7, v7, v8, vcc
	v_add_u32_e32 v8, 1, v3
	v_cmp_ge_u32_e32 vcc, v7, v5
	s_nop 1
	v_cndmask_b32_e32 v3, v3, v8, vcc
	v_mul_lo_u32 v7, v5, v3
	v_add_u32_e32 v5, v7, v5
	v_cmp_ne_u32_e32 vcc, v6, v5
	s_and_saveexec_b64 s[8:9], vcc
	s_xor_b64 s[8:9], exec, s[8:9]
	s_cbranch_execz .LBB0_299
	v_readlane_b32 s4, v253, 57
	v_readlane_b32 s5, v253, 58
	s_waitcnt lgkmcnt(0)
	s_nop 3
	buffer_inv sc1
	global_load_dword v2, v4, s[4:5] sc1
	s_waitcnt vmcnt(0)
	v_cmp_eq_u32_e32 vcc, v2, v3
	s_and_saveexec_b64 s[10:11], vcc
	s_cbranch_execz .LBB0_298
	s_mov_b32 s5, 1
	s_mov_b64 s[12:13], 0
	s_branch .LBB0_289

.LBB0_298:
	s_or_b64 exec, exec, s[10:11]
	s_waitcnt vmcnt(0)
	s_waitcnt vmcnt(0)

.LBB0_468:
	v_readlane_b32 s8, v253, 55
	v_readlane_b32 s9, v253, 56
	v_cvt_f32_u32_e32 v3, v5
	v_sub_u32_e32 v7, 0, v5
	v_rcp_iflag_f32_e32 v3, v3
	s_nop 1
	global_atomic_add v6, v4, v201, s[8:9] sc0
	v_mul_f32_e32 v3, 0x4f7ffffe, v3
	v_cvt_u32_f32_e32 v3, v3
	v_mul_lo_u32 v7, v7, v3
	v_mul_hi_u32 v7, v3, v7
	v_add_u32_e32 v3, v3, v7
	s_waitcnt vmcnt(0)
	v_mul_hi_u32 v3, v6, v3
	v_mul_lo_u32 v7, v3, v5
	v_sub_u32_e32 v7, v6, v7
	v_add_u32_e32 v8, 1, v3
	v_cmp_ge_u32_e32 vcc, v7, v5
	v_add_u32_e32 v6, 1, v6
	s_nop 0
	v_cndmask_b32_e32 v3, v3, v8, vcc
	v_sub_u32_e32 v8, v7, v5
	v_cndmask_b32_e32 v7, v7, v8, vcc
	v_add_u32_e32 v8, 1, v3
	v_cmp_ge_u32_e32 vcc, v7, v5
	s_nop 1
	v_cndmask_b32_e32 v3, v3, v8, vcc
	v_mul_lo_u32 v7, v5, v3
	v_add_u32_e32 v5, v7, v5
	v_cmp_ne_u32_e32 vcc, v6, v5
	s_and_saveexec_b64 s[8:9], vcc
	s_xor_b64 s[8:9], exec, s[8:9]
	s_cbranch_execz .LBB0_482
	v_readlane_b32 s10, v253, 57
	v_readlane_b32 s11, v253, 58
	s_waitcnt lgkmcnt(0)
	s_nop 3
	buffer_inv sc1
	global_load_dword v2, v4, s[10:11] sc1
	s_waitcnt vmcnt(0)
	v_cmp_eq_u32_e32 vcc, v2, v3
	s_and_saveexec_b64 s[10:11], vcc
	s_cbranch_execz .LBB0_481
	s_mov_b32 s40, 1
	s_mov_b64 s[12:13], 0
	s_branch .LBB0_472
